# P7 mid-K gate fold: rolling window of 5 row groups (40 gate loads) in flight in dead VGPRs instead of 32 dependent load-pair round trips per unit; compiler arithmetic kept
# speedup vs baseline: 1.0090x; 1.0090x over previous
; __device__ __forceinline__ int fresh_lane() { int l; asm volatile("v_mbcnt_lo_u32_b32 %0, -1, 0\n\tv_mbcnt_hi_u32_b32 %0, -1, %0" : "=v"(l)); return l; }
; __device__ __forceinline__ float bf_lo(unsigned w) { return __uint_as_float(w << 16); }
; __device__ __forceinline__ float bf_hi(unsigned w) { return __uint_as_float(w & 0xffff0000u); }
;     __device__ __forceinline__ void mid(f32x4 (&acc)[2][2][4][2], const Unit& u, int wr, int wc) const {
;         const int l_ = fresh_lane(), fr = l_ & 15, fq = l_ >> 4;
;         const int row0 = u.pm * BM + wr * 64 + fr, col0 = u.pn * BM + wc * 32 + 4 * fq;
; #pragma unroll
;         for (int ai = 0; ai < 2; ++ai)
; #pragma unroll
;             for (int m = 0; m < 4; ++m) { const size_t r = (size_t)(row0 + ai * HALF + m * 16);
; #pragma unroll
;                 for (int bj = 0; bj < 2; ++bj)
; #pragma unroll
;                     for (int n = 0; n < 2; ++n) { const u32x2 ga = *(const u32x2*)(G + r * ldg + col0 + bj * HALF + n * 16), gb = *(const u32x2*)(G + r * ldg + 4096 + col0 + bj * HALF + n * 16); f32x4 a = acc[ai][bj][m][n];
;                         a[0] *= bf_lo(ga.x) * __builtin_amdgcn_rcpf(bf_lo(gb.x)); a[1] *= bf_hi(ga.x) * __builtin_amdgcn_rcpf(bf_hi(gb.x)); a[2] *= bf_lo(ga.y) * __builtin_amdgcn_rcpf(bf_lo(gb.y)); a[3] *= bf_hi(ga.y) * __builtin_amdgcn_rcpf(bf_hi(gb.y));
;                         acc[ai][bj][m][n] = a; }
;                 asm volatile("" ::: "memory"); }
;     ...
;             if constexpr (Epi::MIDK) { if (t == (nt >> 1)) E.mid(acc, cur, wr, wc); }
.LBB0_2990:
	s_cmpk_lg_i32 s52, 0x800
	s_cbranch_scc1 .LBB0_2989
	v_mbcnt_lo_u32_b32 v135, -1, 0
	v_mbcnt_hi_u32_b32 v135, -1, v135
	s_mov_b64 s[54:55], 0x200000
	v_ashrrev_i32_e32 v134, 2, v135
	v_and_or_b32 v135, v135, 15, s74
	v_and_b32_e32 v134, -4, v134
	v_add_u32_e32 v142, s87, v135
	v_add_u32_e32 v134, s43, v134
	v_ashrrev_i32_e32 v143, 31, v142
	v_ashrrev_i32_e32 v135, 31, v134
	v_lshlrev_b64 v[136:137], 14, v[142:143]
	v_lshl_add_u64 v[136:137], s[12:13], 0, v[136:137]
	v_lshlrev_b64 v[144:145], 1, v[134:135]
	v_lshl_add_u64 v[140:141], v[136:137], 0, v[144:145]
	v_add_co_u32_e32 v146, vcc, s66, v140
	v_mov_b32_e32 v236, v142
	v_ashrrev_i32_e32 v237, 31, v236
	v_lshlrev_b64 v[236:237], 14, v[236:237]
	v_lshl_add_u64 v[236:237], s[12:13], 0, v[236:237]
	v_lshl_add_u64 v[236:237], v[236:237], 0, v[144:145]
	v_add_co_u32_e32 v238, vcc, s66, v236
	s_nop 1
	v_addc_co_u32_e32 v239, vcc, 0, v237, vcc
	global_load_dwordx2 v[156:157], v[236:237], off
	global_load_dwordx2 v[158:159], v[238:239], off
	global_load_dwordx2 v[160:161], v[236:237], off offset:32
	global_load_dwordx2 v[162:163], v[238:239], off offset:32
	global_load_dwordx2 v[164:165], v[236:237], off offset:256
	global_load_dwordx2 v[166:167], v[238:239], off offset:256
	global_load_dwordx2 v[168:169], v[236:237], off offset:288
	global_load_dwordx2 v[170:171], v[238:239], off offset:288
	v_or_b32_e32 v236, 16, v142
	v_ashrrev_i32_e32 v237, 31, v236
	v_lshlrev_b64 v[236:237], 14, v[236:237]
	v_lshl_add_u64 v[236:237], s[12:13], 0, v[236:237]
	v_lshl_add_u64 v[236:237], v[236:237], 0, v[144:145]
	v_add_co_u32_e32 v238, vcc, s66, v236
	s_nop 1
	v_addc_co_u32_e32 v239, vcc, 0, v237, vcc
	global_load_dwordx2 v[172:173], v[236:237], off
	global_load_dwordx2 v[174:175], v[238:239], off
	global_load_dwordx2 v[176:177], v[236:237], off offset:32
	global_load_dwordx2 v[178:179], v[238:239], off offset:32
	global_load_dwordx2 v[180:181], v[236:237], off offset:256
	global_load_dwordx2 v[182:183], v[238:239], off offset:256
	global_load_dwordx2 v[184:185], v[236:237], off offset:288
	global_load_dwordx2 v[186:187], v[238:239], off offset:288
	v_or_b32_e32 v236, 32, v142
	v_ashrrev_i32_e32 v237, 31, v236
	v_lshlrev_b64 v[236:237], 14, v[236:237]
	v_lshl_add_u64 v[236:237], s[12:13], 0, v[236:237]
	v_lshl_add_u64 v[236:237], v[236:237], 0, v[144:145]
	v_add_co_u32_e32 v238, vcc, s66, v236
	s_nop 1
	v_addc_co_u32_e32 v239, vcc, 0, v237, vcc
	global_load_dwordx2 v[188:189], v[236:237], off
	global_load_dwordx2 v[190:191], v[238:239], off
	global_load_dwordx2 v[192:193], v[236:237], off offset:32
	global_load_dwordx2 v[194:195], v[238:239], off offset:32
	global_load_dwordx2 v[196:197], v[236:237], off offset:256
	global_load_dwordx2 v[198:199], v[238:239], off offset:256
	global_load_dwordx2 v[200:201], v[236:237], off offset:288
	global_load_dwordx2 v[202:203], v[238:239], off offset:288
	v_or_b32_e32 v236, 48, v142
	v_ashrrev_i32_e32 v237, 31, v236
	v_lshlrev_b64 v[236:237], 14, v[236:237]
	v_lshl_add_u64 v[236:237], s[12:13], 0, v[236:237]
	v_lshl_add_u64 v[236:237], v[236:237], 0, v[144:145]
	v_add_co_u32_e32 v238, vcc, s66, v236
	s_nop 1
	v_addc_co_u32_e32 v239, vcc, 0, v237, vcc
	global_load_dwordx2 v[204:205], v[236:237], off
	global_load_dwordx2 v[206:207], v[238:239], off
	global_load_dwordx2 v[208:209], v[236:237], off offset:32
	global_load_dwordx2 v[210:211], v[238:239], off offset:32
	global_load_dwordx2 v[212:213], v[236:237], off offset:256
	global_load_dwordx2 v[214:215], v[238:239], off offset:256
	global_load_dwordx2 v[216:217], v[236:237], off offset:288
	global_load_dwordx2 v[218:219], v[238:239], off offset:288
	v_or_b32_e32 v236, 128, v142
	v_ashrrev_i32_e32 v237, 31, v236
	v_lshlrev_b64 v[236:237], 14, v[236:237]
	v_lshl_add_u64 v[236:237], s[12:13], 0, v[236:237]
	v_lshl_add_u64 v[236:237], v[236:237], 0, v[144:145]
	v_add_co_u32_e32 v238, vcc, s66, v236
	s_nop 1
	v_addc_co_u32_e32 v239, vcc, 0, v237, vcc
	global_load_dwordx2 v[220:221], v[236:237], off
	global_load_dwordx2 v[222:223], v[238:239], off
	global_load_dwordx2 v[224:225], v[236:237], off offset:32
	global_load_dwordx2 v[226:227], v[238:239], off offset:32
	global_load_dwordx2 v[228:229], v[236:237], off offset:256
	global_load_dwordx2 v[230:231], v[238:239], off offset:256
	global_load_dwordx2 v[232:233], v[236:237], off offset:288
	global_load_dwordx2 v[234:235], v[238:239], off offset:288
	s_waitcnt vmcnt(39)
	v_mov_b64_e32 v[134:135], v[156:157]
	s_nop 0
	v_addc_co_u32_e32 v147, vcc, 0, v141, vcc
	s_waitcnt vmcnt(38)
	v_mov_b64_e32 v[136:137], v[158:159]
	v_lshlrev_b32_e32 v152, 16, v134
	v_and_b32_e32 v153, 0xffff0000, v134
	v_lshlrev_b32_e32 v143, 16, v136
	v_and_b32_e32 v136, 0xffff0000, v136
	v_lshlrev_b32_e32 v134, 16, v137
	v_rcp_f32_e32 v149, v136
	v_rcp_f32_e32 v136, v134
	v_and_b32_e32 v134, 0xffff0000, v137
	v_rcp_f32_e32 v137, v134
	v_lshlrev_b32_e32 v134, 16, v135
	v_and_b32_e32 v135, 0xffff0000, v135
	v_rcp_f32_e32 v148, v143
	v_pk_mul_f32 v[134:135], v[136:137], v[134:135]
	v_pk_mul_f32 v[148:149], v[148:149], v[152:153]
	v_pk_mul_f32 v[128:129], v[128:129], v[134:135]
	s_waitcnt vmcnt(37)
	v_mov_b64_e32 v[134:135], v[160:161]
	s_waitcnt vmcnt(36)
	v_mov_b64_e32 v[136:137], v[162:163]
	v_pk_mul_f32 v[126:127], v[126:127], v[148:149]
	v_lshlrev_b32_e32 v152, 16, v134
	v_lshlrev_b32_e32 v143, 16, v136
	v_and_b32_e32 v136, 0xffff0000, v136
	v_and_b32_e32 v153, 0xffff0000, v134
	v_lshlrev_b32_e32 v134, 16, v137
	v_rcp_f32_e32 v149, v136
	v_rcp_f32_e32 v136, v134
	v_and_b32_e32 v134, 0xffff0000, v137
	v_rcp_f32_e32 v137, v134
	v_lshlrev_b32_e32 v134, 16, v135
	v_and_b32_e32 v135, 0xffff0000, v135
	v_rcp_f32_e32 v148, v143
	v_pk_mul_f32 v[134:135], v[136:137], v[134:135]
	v_pk_mul_f32 v[148:149], v[148:149], v[152:153]
	v_pk_mul_f32 v[124:125], v[124:125], v[134:135]
	s_waitcnt vmcnt(35)
; __device__ __forceinline__ float bf_lo(unsigned w) { return __uint_as_float(w << 16); }
; __device__ __forceinline__ float bf_hi(unsigned w) { return __uint_as_float(w & 0xffff0000u); }
;     __device__ __forceinline__ void mid(f32x4 (&acc)[2][2][4][2], const Unit& u, int wr, int wc) const {
;     ...
;             for (int m = 0; m < 4; ++m) { const size_t r = (size_t)(row0 + ai * HALF + m * 16);
; #pragma unroll
;                 for (int bj = 0; bj < 2; ++bj)
; #pragma unroll
;                     for (int n = 0; n < 2; ++n) { const u32x2 ga = *(const u32x2*)(G + r * ldg + col0 + bj * HALF + n * 16), gb = *(const u32x2*)(G + r * ldg + 4096 + col0 + bj * HALF + n * 16); f32x4 a = acc[ai][bj][m][n];
;                         a[0] *= bf_lo(ga.x) * __builtin_amdgcn_rcpf(bf_lo(gb.x)); a[1] *= bf_hi(ga.x) * __builtin_amdgcn_rcpf(bf_hi(gb.x)); a[2] *= bf_lo(ga.y) * __builtin_amdgcn_rcpf(bf_lo(gb.y)); a[3] *= bf_hi(ga.y) * __builtin_amdgcn_rcpf(bf_hi(gb.y));
;                         acc[ai][bj][m][n] = a; }
	v_mov_b64_e32 v[134:135], v[164:165]
	s_waitcnt vmcnt(34)
	v_mov_b64_e32 v[136:137], v[166:167]
	v_pk_mul_f32 v[122:123], v[122:123], v[148:149]
	v_lshlrev_b32_e32 v152, 16, v134
	v_lshlrev_b32_e32 v143, 16, v136
	v_and_b32_e32 v136, 0xffff0000, v136
	v_and_b32_e32 v153, 0xffff0000, v134
	v_lshlrev_b32_e32 v134, 16, v137
	v_rcp_f32_e32 v149, v136
	v_rcp_f32_e32 v136, v134
	v_and_b32_e32 v134, 0xffff0000, v137
	v_rcp_f32_e32 v137, v134
	v_lshlrev_b32_e32 v134, 16, v135
	v_and_b32_e32 v135, 0xffff0000, v135
	v_rcp_f32_e32 v148, v143
	v_pk_mul_f32 v[134:135], v[136:137], v[134:135]
	v_pk_mul_f32 v[148:149], v[148:149], v[152:153]
	v_pk_mul_f32 v[120:121], v[120:121], v[134:135]
	s_waitcnt vmcnt(33)
	v_mov_b64_e32 v[134:135], v[168:169]
	s_waitcnt vmcnt(32)
	v_mov_b64_e32 v[136:137], v[170:171]
	v_or_b32_e32 v236, 144, v142
	v_ashrrev_i32_e32 v237, 31, v236
	v_lshlrev_b64 v[236:237], 14, v[236:237]
	v_lshl_add_u64 v[236:237], s[12:13], 0, v[236:237]
	v_lshl_add_u64 v[236:237], v[236:237], 0, v[144:145]
	v_add_co_u32_e32 v238, vcc, s66, v236
	s_nop 1
	v_addc_co_u32_e32 v239, vcc, 0, v237, vcc
	global_load_dwordx2 v[156:157], v[236:237], off
	global_load_dwordx2 v[158:159], v[238:239], off
	global_load_dwordx2 v[160:161], v[236:237], off offset:32
	global_load_dwordx2 v[162:163], v[238:239], off offset:32
	global_load_dwordx2 v[164:165], v[236:237], off offset:256
	global_load_dwordx2 v[166:167], v[238:239], off offset:256
	global_load_dwordx2 v[168:169], v[236:237], off offset:288
	global_load_dwordx2 v[170:171], v[238:239], off offset:288
	v_pk_mul_f32 v[118:119], v[118:119], v[148:149]
	v_lshlrev_b32_e32 v148, 16, v134
	v_lshlrev_b32_e32 v143, 16, v136
	v_and_b32_e32 v136, 0xffff0000, v136
	v_and_b32_e32 v149, 0xffff0000, v134
	v_lshlrev_b32_e32 v134, 16, v137
	v_rcp_f32_e32 v147, v136
	v_rcp_f32_e32 v136, v134
	v_and_b32_e32 v134, 0xffff0000, v137
	v_rcp_f32_e32 v137, v134
	v_lshlrev_b32_e32 v134, 16, v135
	v_and_b32_e32 v135, 0xffff0000, v135
	v_rcp_f32_e32 v146, v143
	v_pk_mul_f32 v[134:135], v[136:137], v[134:135]
	v_pk_mul_f32 v[146:147], v[146:147], v[148:149]
	v_pk_mul_f32 v[116:117], v[116:117], v[134:135]
	v_or_b32_e32 v134, 16, v142
	v_ashrrev_i32_e32 v135, 31, v134
	v_lshlrev_b64 v[134:135], 14, v[134:135]
	v_lshl_add_u64 v[134:135], s[12:13], 0, v[134:135]
	v_lshl_add_u64 v[134:135], v[134:135], 0, v[144:145]
	v_pk_mul_f32 v[114:115], v[114:115], v[146:147]
	v_add_co_u32_e32 v146, vcc, s66, v134
	s_waitcnt vmcnt(39)
	v_mov_b64_e32 v[136:137], v[172:173]
	s_nop 0
	v_addc_co_u32_e32 v147, vcc, 0, v135, vcc
	s_waitcnt vmcnt(38)
	v_mov_b64_e32 v[148:149], v[174:175]
	v_lshlrev_b32_e32 v154, 16, v136
	v_and_b32_e32 v155, 0xffff0000, v136
	v_lshlrev_b32_e32 v143, 16, v148
	v_lshlrev_b32_e32 v136, 16, v149
	v_rcp_f32_e32 v152, v143
	v_and_b32_e32 v143, 0xffff0000, v148
	v_rcp_f32_e32 v148, v136
	v_and_b32_e32 v136, 0xffff0000, v149
	v_rcp_f32_e32 v149, v136
	v_lshlrev_b32_e32 v136, 16, v137
	v_and_b32_e32 v137, 0xffff0000, v137
	v_rcp_f32_e32 v153, v143
	v_pk_mul_f32 v[136:137], v[148:149], v[136:137]
	v_pk_mul_f32 v[152:153], v[152:153], v[154:155]
	v_pk_mul_f32 v[112:113], v[112:113], v[136:137]
	s_waitcnt vmcnt(37)
	v_mov_b64_e32 v[136:137], v[176:177]
	s_waitcnt vmcnt(36)
	v_mov_b64_e32 v[148:149], v[178:179]
	v_pk_mul_f32 v[110:111], v[110:111], v[152:153]
	v_lshlrev_b32_e32 v154, 16, v136
	v_lshlrev_b32_e32 v143, 16, v148
	v_and_b32_e32 v155, 0xffff0000, v136
	v_lshlrev_b32_e32 v136, 16, v149
	v_rcp_f32_e32 v152, v143
	v_and_b32_e32 v143, 0xffff0000, v148
	v_rcp_f32_e32 v148, v136
	v_and_b32_e32 v136, 0xffff0000, v149
	v_rcp_f32_e32 v149, v136
	v_lshlrev_b32_e32 v136, 16, v137
	v_and_b32_e32 v137, 0xffff0000, v137
	v_rcp_f32_e32 v153, v143
	v_pk_mul_f32 v[136:137], v[148:149], v[136:137]
	v_pk_mul_f32 v[152:153], v[152:153], v[154:155]
	v_pk_mul_f32 v[108:109], v[108:109], v[136:137]
	s_waitcnt vmcnt(35)
	v_mov_b64_e32 v[136:137], v[180:181]
	s_waitcnt vmcnt(34)
	v_mov_b64_e32 v[148:149], v[182:183]
	v_pk_mul_f32 v[106:107], v[106:107], v[152:153]
	v_lshlrev_b32_e32 v154, 16, v136
	v_lshlrev_b32_e32 v143, 16, v148
	v_and_b32_e32 v155, 0xffff0000, v136
	v_lshlrev_b32_e32 v136, 16, v149
	v_rcp_f32_e32 v152, v143
	v_and_b32_e32 v143, 0xffff0000, v148
	v_rcp_f32_e32 v148, v136
	v_and_b32_e32 v136, 0xffff0000, v149
	v_rcp_f32_e32 v149, v136
	v_lshlrev_b32_e32 v136, 16, v137
	v_and_b32_e32 v137, 0xffff0000, v137
	v_rcp_f32_e32 v153, v143
	v_pk_mul_f32 v[136:137], v[148:149], v[136:137]
	v_pk_mul_f32 v[152:153], v[152:153], v[154:155]
	v_pk_mul_f32 v[104:105], v[104:105], v[136:137]
	s_waitcnt vmcnt(33)
	v_mov_b64_e32 v[134:135], v[184:185]
	s_nop 0
	s_waitcnt vmcnt(32)
	v_mov_b64_e32 v[136:137], v[186:187]
	v_or_b32_e32 v236, 160, v142
	v_ashrrev_i32_e32 v237, 31, v236
	v_lshlrev_b64 v[236:237], 14, v[236:237]
	v_lshl_add_u64 v[236:237], s[12:13], 0, v[236:237]
	v_lshl_add_u64 v[236:237], v[236:237], 0, v[144:145]
	v_add_co_u32_e32 v238, vcc, s66, v236
	s_nop 1
	v_addc_co_u32_e32 v239, vcc, 0, v237, vcc
	global_load_dwordx2 v[172:173], v[236:237], off
	global_load_dwordx2 v[174:175], v[238:239], off
	global_load_dwordx2 v[176:177], v[236:237], off offset:32
	global_load_dwordx2 v[178:179], v[238:239], off offset:32
	global_load_dwordx2 v[180:181], v[236:237], off offset:256
	global_load_dwordx2 v[182:183], v[238:239], off offset:256
	global_load_dwordx2 v[184:185], v[236:237], off offset:288
	global_load_dwordx2 v[186:187], v[238:239], off offset:288
	v_pk_mul_f32 v[102:103], v[102:103], v[152:153]
	v_lshlrev_b32_e32 v148, 16, v134
	v_lshlrev_b32_e32 v143, 16, v136
	v_and_b32_e32 v136, 0xffff0000, v136
	v_and_b32_e32 v149, 0xffff0000, v134
	v_lshlrev_b32_e32 v134, 16, v137
	v_rcp_f32_e32 v147, v136
	v_rcp_f32_e32 v136, v134
	v_and_b32_e32 v134, 0xffff0000, v137
	v_rcp_f32_e32 v137, v134
	v_lshlrev_b32_e32 v134, 16, v135
	v_and_b32_e32 v135, 0xffff0000, v135
	v_rcp_f32_e32 v146, v143
	v_pk_mul_f32 v[134:135], v[136:137], v[134:135]
	v_pk_mul_f32 v[146:147], v[146:147], v[148:149]
	v_pk_mul_f32 v[100:101], v[100:101], v[134:135]
	v_or_b32_e32 v134, 32, v142
	v_ashrrev_i32_e32 v135, 31, v134
	v_lshlrev_b64 v[134:135], 14, v[134:135]
	v_lshl_add_u64 v[134:135], s[12:13], 0, v[134:135]
	v_lshl_add_u64 v[148:149], v[134:135], 0, v[144:145]
	v_pk_mul_f32 v[98:99], v[98:99], v[146:147]
	v_add_co_u32_e32 v146, vcc, s66, v148
	s_waitcnt vmcnt(39)
; __device__ __forceinline__ float bf_lo(unsigned w) { return __uint_as_float(w << 16); }
; __device__ __forceinline__ float bf_hi(unsigned w) { return __uint_as_float(w & 0xffff0000u); }
;     __device__ __forceinline__ void mid(f32x4 (&acc)[2][2][4][2], const Unit& u, int wr, int wc) const {
;     ...
;             for (int m = 0; m < 4; ++m) { const size_t r = (size_t)(row0 + ai * HALF + m * 16);
; #pragma unroll
;                 for (int bj = 0; bj < 2; ++bj)
; #pragma unroll
;                     for (int n = 0; n < 2; ++n) { const u32x2 ga = *(const u32x2*)(G + r * ldg + col0 + bj * HALF + n * 16), gb = *(const u32x2*)(G + r * ldg + 4096 + col0 + bj * HALF + n * 16); f32x4 a = acc[ai][bj][m][n];
;                         a[0] *= bf_lo(ga.x) * __builtin_amdgcn_rcpf(bf_lo(gb.x)); a[1] *= bf_hi(ga.x) * __builtin_amdgcn_rcpf(bf_hi(gb.x)); a[2] *= bf_lo(ga.y) * __builtin_amdgcn_rcpf(bf_lo(gb.y)); a[3] *= bf_hi(ga.y) * __builtin_amdgcn_rcpf(bf_hi(gb.y));
;                         acc[ai][bj][m][n] = a; }
	v_mov_b64_e32 v[134:135], v[188:189]
	s_nop 0
	v_addc_co_u32_e32 v147, vcc, 0, v149, vcc
	s_waitcnt vmcnt(38)
	v_mov_b64_e32 v[136:137], v[190:191]
	v_lshlrev_b32_e32 v154, 16, v134
	v_and_b32_e32 v155, 0xffff0000, v134
	v_lshlrev_b32_e32 v143, 16, v136
	v_and_b32_e32 v136, 0xffff0000, v136
	v_lshlrev_b32_e32 v134, 16, v137
	v_rcp_f32_e32 v153, v136
	v_rcp_f32_e32 v136, v134
	v_and_b32_e32 v134, 0xffff0000, v137
	v_rcp_f32_e32 v137, v134
	v_lshlrev_b32_e32 v134, 16, v135
	v_and_b32_e32 v135, 0xffff0000, v135
	v_rcp_f32_e32 v152, v143
	v_pk_mul_f32 v[134:135], v[136:137], v[134:135]
	v_pk_mul_f32 v[152:153], v[152:153], v[154:155]
	v_pk_mul_f32 v[96:97], v[96:97], v[134:135]
	s_waitcnt vmcnt(37)
	v_mov_b64_e32 v[134:135], v[192:193]
	s_waitcnt vmcnt(36)
	v_mov_b64_e32 v[136:137], v[194:195]
	v_pk_mul_f32 v[94:95], v[94:95], v[152:153]
	v_lshlrev_b32_e32 v154, 16, v134
	v_lshlrev_b32_e32 v143, 16, v136
	v_and_b32_e32 v136, 0xffff0000, v136
	v_and_b32_e32 v155, 0xffff0000, v134
	v_lshlrev_b32_e32 v134, 16, v137
	v_rcp_f32_e32 v153, v136
	v_rcp_f32_e32 v136, v134
	v_and_b32_e32 v134, 0xffff0000, v137
	v_rcp_f32_e32 v137, v134
	v_lshlrev_b32_e32 v134, 16, v135
	v_and_b32_e32 v135, 0xffff0000, v135
	v_rcp_f32_e32 v152, v143
	v_pk_mul_f32 v[134:135], v[136:137], v[134:135]
	v_pk_mul_f32 v[152:153], v[152:153], v[154:155]
	v_pk_mul_f32 v[92:93], v[92:93], v[134:135]
	s_waitcnt vmcnt(35)
	v_mov_b64_e32 v[134:135], v[196:197]
	s_waitcnt vmcnt(34)
	v_mov_b64_e32 v[136:137], v[198:199]
	v_pk_mul_f32 v[90:91], v[90:91], v[152:153]
	v_lshlrev_b32_e32 v154, 16, v134
	v_lshlrev_b32_e32 v143, 16, v136
	v_and_b32_e32 v136, 0xffff0000, v136
	v_and_b32_e32 v155, 0xffff0000, v134
	v_lshlrev_b32_e32 v134, 16, v137
	v_rcp_f32_e32 v153, v136
	v_rcp_f32_e32 v136, v134
	v_and_b32_e32 v134, 0xffff0000, v137
	v_rcp_f32_e32 v137, v134
	v_lshlrev_b32_e32 v134, 16, v135
	v_and_b32_e32 v135, 0xffff0000, v135
	v_rcp_f32_e32 v152, v143
	v_pk_mul_f32 v[134:135], v[136:137], v[134:135]
	v_pk_mul_f32 v[152:153], v[152:153], v[154:155]
	v_pk_mul_f32 v[88:89], v[88:89], v[134:135]
	s_waitcnt vmcnt(33)
	v_mov_b64_e32 v[134:135], v[200:201]
	s_waitcnt vmcnt(32)
	v_mov_b64_e32 v[136:137], v[202:203]
	v_or_b32_e32 v236, 176, v142
	v_ashrrev_i32_e32 v237, 31, v236
	v_lshlrev_b64 v[236:237], 14, v[236:237]
	v_lshl_add_u64 v[236:237], s[12:13], 0, v[236:237]
	v_lshl_add_u64 v[236:237], v[236:237], 0, v[144:145]
	v_add_co_u32_e32 v238, vcc, s66, v236
	s_nop 1
	v_addc_co_u32_e32 v239, vcc, 0, v237, vcc
	global_load_dwordx2 v[188:189], v[236:237], off
	global_load_dwordx2 v[190:191], v[238:239], off
	global_load_dwordx2 v[192:193], v[236:237], off offset:32
	global_load_dwordx2 v[194:195], v[238:239], off offset:32
	global_load_dwordx2 v[196:197], v[236:237], off offset:256
	global_load_dwordx2 v[198:199], v[238:239], off offset:256
	global_load_dwordx2 v[200:201], v[236:237], off offset:288
	global_load_dwordx2 v[202:203], v[238:239], off offset:288
	v_pk_mul_f32 v[86:87], v[86:87], v[152:153]
	v_lshlrev_b32_e32 v148, 16, v134
	v_lshlrev_b32_e32 v143, 16, v136
	v_and_b32_e32 v136, 0xffff0000, v136
	v_and_b32_e32 v149, 0xffff0000, v134
	v_lshlrev_b32_e32 v134, 16, v137
	v_rcp_f32_e32 v147, v136
	v_rcp_f32_e32 v136, v134
	v_and_b32_e32 v134, 0xffff0000, v137
	v_rcp_f32_e32 v137, v134
	v_lshlrev_b32_e32 v134, 16, v135
	v_and_b32_e32 v135, 0xffff0000, v135
	v_rcp_f32_e32 v146, v143
	v_pk_mul_f32 v[134:135], v[136:137], v[134:135]
	v_pk_mul_f32 v[146:147], v[146:147], v[148:149]
	v_pk_mul_f32 v[84:85], v[84:85], v[134:135]
	v_or_b32_e32 v134, 48, v142
	v_ashrrev_i32_e32 v135, 31, v134
	v_lshlrev_b64 v[134:135], 14, v[134:135]
	v_lshl_add_u64 v[134:135], s[12:13], 0, v[134:135]
	v_lshl_add_u64 v[144:145], v[134:135], 0, v[144:145]
	v_add_co_u32_e32 v142, vcc, s66, v144
	s_waitcnt vmcnt(39)
	v_mov_b64_e32 v[134:135], v[204:205]
	s_nop 0
	v_addc_co_u32_e32 v143, vcc, 0, v145, vcc
	s_waitcnt vmcnt(38)
	v_mov_b64_e32 v[136:137], v[206:207]
	v_pk_mul_f32 v[82:83], v[82:83], v[146:147]
	v_lshlrev_b32_e32 v148, 16, v134
	v_and_b32_e32 v149, 0xffff0000, v134
	v_lshlrev_b32_e32 v146, 16, v136
	v_and_b32_e32 v136, 0xffff0000, v136
	v_lshlrev_b32_e32 v134, 16, v137
	v_rcp_f32_e32 v147, v136
	v_rcp_f32_e32 v136, v134
	v_and_b32_e32 v134, 0xffff0000, v137
	v_rcp_f32_e32 v137, v134
	v_lshlrev_b32_e32 v134, 16, v135
	v_and_b32_e32 v135, 0xffff0000, v135
	v_rcp_f32_e32 v146, v146
	v_pk_mul_f32 v[134:135], v[136:137], v[134:135]
	v_pk_mul_f32 v[146:147], v[146:147], v[148:149]
	v_pk_mul_f32 v[80:81], v[80:81], v[134:135]
	s_waitcnt vmcnt(37)
	v_mov_b64_e32 v[134:135], v[208:209]
	s_waitcnt vmcnt(36)
	v_mov_b64_e32 v[136:137], v[210:211]
	v_pk_mul_f32 v[78:79], v[78:79], v[146:147]
	v_lshlrev_b32_e32 v148, 16, v134
	v_lshlrev_b32_e32 v146, 16, v136
	v_and_b32_e32 v136, 0xffff0000, v136
	v_and_b32_e32 v149, 0xffff0000, v134
	v_lshlrev_b32_e32 v134, 16, v137
	v_rcp_f32_e32 v147, v136
	v_rcp_f32_e32 v136, v134
	v_and_b32_e32 v134, 0xffff0000, v137
	v_rcp_f32_e32 v137, v134
	v_lshlrev_b32_e32 v134, 16, v135
	v_and_b32_e32 v135, 0xffff0000, v135
	v_rcp_f32_e32 v146, v146
	v_pk_mul_f32 v[134:135], v[136:137], v[134:135]
	v_pk_mul_f32 v[146:147], v[146:147], v[148:149]
	v_pk_mul_f32 v[76:77], v[76:77], v[134:135]
	s_waitcnt vmcnt(35)
	v_mov_b64_e32 v[134:135], v[212:213]
	s_waitcnt vmcnt(34)
	v_mov_b64_e32 v[136:137], v[214:215]
	v_pk_mul_f32 v[74:75], v[74:75], v[146:147]
	v_lshlrev_b32_e32 v148, 16, v134
	v_lshlrev_b32_e32 v146, 16, v136
	v_and_b32_e32 v136, 0xffff0000, v136
	v_and_b32_e32 v149, 0xffff0000, v134
	v_lshlrev_b32_e32 v134, 16, v137
	v_rcp_f32_e32 v147, v136
	v_rcp_f32_e32 v136, v134
	v_and_b32_e32 v134, 0xffff0000, v137
	v_rcp_f32_e32 v137, v134
	v_lshlrev_b32_e32 v134, 16, v135
	v_and_b32_e32 v135, 0xffff0000, v135
	v_rcp_f32_e32 v146, v146
	v_pk_mul_f32 v[134:135], v[136:137], v[134:135]
	v_pk_mul_f32 v[146:147], v[146:147], v[148:149]
	v_pk_mul_f32 v[72:73], v[72:73], v[134:135]
	s_waitcnt vmcnt(33)
; __device__ __forceinline__ float bf_lo(unsigned w) { return __uint_as_float(w << 16); }
; __device__ __forceinline__ float bf_hi(unsigned w) { return __uint_as_float(w & 0xffff0000u); }
;     __device__ __forceinline__ void mid(f32x4 (&acc)[2][2][4][2], const Unit& u, int wr, int wc) const {
;     ...
;             for (int m = 0; m < 4; ++m) { const size_t r = (size_t)(row0 + ai * HALF + m * 16);
; #pragma unroll
;                 for (int bj = 0; bj < 2; ++bj)
; #pragma unroll
;                     for (int n = 0; n < 2; ++n) { const u32x2 ga = *(const u32x2*)(G + r * ldg + col0 + bj * HALF + n * 16), gb = *(const u32x2*)(G + r * ldg + 4096 + col0 + bj * HALF + n * 16); f32x4 a = acc[ai][bj][m][n];
;                         a[0] *= bf_lo(ga.x) * __builtin_amdgcn_rcpf(bf_lo(gb.x)); a[1] *= bf_hi(ga.x) * __builtin_amdgcn_rcpf(bf_hi(gb.x)); a[2] *= bf_lo(ga.y) * __builtin_amdgcn_rcpf(bf_lo(gb.y)); a[3] *= bf_hi(ga.y) * __builtin_amdgcn_rcpf(bf_hi(gb.y));
;                         acc[ai][bj][m][n] = a; }
	v_mov_b64_e32 v[134:135], v[216:217]
	s_waitcnt vmcnt(32)
	v_mov_b64_e32 v[136:137], v[218:219]
	v_pk_mul_f32 v[70:71], v[70:71], v[146:147]
	v_lshlrev_b32_e32 v144, 16, v134
	v_lshlrev_b32_e32 v142, 16, v136
	v_and_b32_e32 v136, 0xffff0000, v136
	v_and_b32_e32 v145, 0xffff0000, v134
	v_lshlrev_b32_e32 v134, 16, v137
	v_rcp_f32_e32 v143, v136
	v_rcp_f32_e32 v136, v134
	v_and_b32_e32 v134, 0xffff0000, v137
	v_rcp_f32_e32 v142, v142
	v_rcp_f32_e32 v137, v134
	v_lshlrev_b32_e32 v134, 16, v135
	v_and_b32_e32 v135, 0xffff0000, v135
	v_pk_mul_f32 v[142:143], v[142:143], v[144:145]
	v_pk_mul_f32 v[134:135], v[136:137], v[134:135]
	v_lshl_add_u64 v[144:145], v[140:141], 0, s[54:55]
	s_mov_b32 s54, 0x200000
	v_pk_mul_f32 v[68:69], v[68:69], v[134:135]
	v_add_co_u32_e32 v134, vcc, s54, v140
	v_pk_mul_f32 v[66:67], v[66:67], v[142:143]
	s_nop 0
	v_addc_co_u32_e32 v135, vcc, 0, v141, vcc
	v_add_co_u32_e32 v142, vcc, s77, v140
	s_waitcnt vmcnt(31)
	v_mov_b64_e32 v[134:135], v[220:221]
	s_nop 0
	v_addc_co_u32_e32 v143, vcc, 0, v141, vcc
	s_waitcnt vmcnt(30)
	v_mov_b64_e32 v[136:137], v[222:223]
	v_lshlrev_b32_e32 v148, 16, v134
	v_and_b32_e32 v149, 0xffff0000, v134
	v_lshlrev_b32_e32 v146, 16, v136
	v_and_b32_e32 v136, 0xffff0000, v136
	v_lshlrev_b32_e32 v134, 16, v137
	v_rcp_f32_e32 v147, v136
	v_rcp_f32_e32 v136, v134
	v_and_b32_e32 v134, 0xffff0000, v137
	v_rcp_f32_e32 v137, v134
	v_lshlrev_b32_e32 v134, 16, v135
	v_and_b32_e32 v135, 0xffff0000, v135
	v_rcp_f32_e32 v146, v146
	v_pk_mul_f32 v[134:135], v[136:137], v[134:135]
	v_pk_mul_f32 v[146:147], v[146:147], v[148:149]
	v_pk_mul_f32 v[64:65], v[64:65], v[134:135]
	s_waitcnt vmcnt(29)
	v_mov_b64_e32 v[134:135], v[224:225]
	s_waitcnt vmcnt(28)
	v_mov_b64_e32 v[136:137], v[226:227]
	v_pk_mul_f32 v[62:63], v[62:63], v[146:147]
	v_lshlrev_b32_e32 v148, 16, v134
	v_lshlrev_b32_e32 v146, 16, v136
	v_and_b32_e32 v136, 0xffff0000, v136
	v_and_b32_e32 v149, 0xffff0000, v134
	v_lshlrev_b32_e32 v134, 16, v137
	v_rcp_f32_e32 v147, v136
	v_rcp_f32_e32 v136, v134
	v_and_b32_e32 v134, 0xffff0000, v137
	v_rcp_f32_e32 v137, v134
	v_lshlrev_b32_e32 v134, 16, v135
	v_and_b32_e32 v135, 0xffff0000, v135
	v_rcp_f32_e32 v146, v146
	v_pk_mul_f32 v[134:135], v[136:137], v[134:135]
	v_pk_mul_f32 v[146:147], v[146:147], v[148:149]
	v_pk_mul_f32 v[60:61], v[60:61], v[134:135]
	s_waitcnt vmcnt(27)
	v_mov_b64_e32 v[134:135], v[228:229]
	s_waitcnt vmcnt(26)
	v_mov_b64_e32 v[136:137], v[230:231]
	v_pk_mul_f32 v[58:59], v[58:59], v[146:147]
	v_lshlrev_b32_e32 v148, 16, v134
	v_lshlrev_b32_e32 v146, 16, v136
	v_and_b32_e32 v136, 0xffff0000, v136
	v_and_b32_e32 v149, 0xffff0000, v134
	v_lshlrev_b32_e32 v134, 16, v137
	v_rcp_f32_e32 v147, v136
	v_rcp_f32_e32 v136, v134
	v_and_b32_e32 v134, 0xffff0000, v137
	v_rcp_f32_e32 v137, v134
	v_lshlrev_b32_e32 v134, 16, v135
	v_and_b32_e32 v135, 0xffff0000, v135
	v_rcp_f32_e32 v146, v146
	v_pk_mul_f32 v[134:135], v[136:137], v[134:135]
	v_pk_mul_f32 v[146:147], v[146:147], v[148:149]
	v_pk_mul_f32 v[56:57], v[56:57], v[134:135]
	s_waitcnt vmcnt(25)
	v_mov_b64_e32 v[134:135], v[232:233]
	s_waitcnt vmcnt(24)
	v_mov_b64_e32 v[136:137], v[234:235]
	v_pk_mul_f32 v[54:55], v[54:55], v[146:147]
	v_lshlrev_b32_e32 v144, 16, v134
	v_lshlrev_b32_e32 v142, 16, v136
	v_and_b32_e32 v136, 0xffff0000, v136
	v_and_b32_e32 v145, 0xffff0000, v134
	v_lshlrev_b32_e32 v134, 16, v137
	v_rcp_f32_e32 v143, v136
	v_rcp_f32_e32 v136, v134
	v_and_b32_e32 v134, 0xffff0000, v137
	v_rcp_f32_e32 v137, v134
	v_rcp_f32_e32 v142, v142
	v_lshlrev_b32_e32 v134, 16, v135
	v_and_b32_e32 v135, 0xffff0000, v135
	v_pk_mul_f32 v[134:135], v[136:137], v[134:135]
	v_pk_mul_f32 v[142:143], v[142:143], v[144:145]
	v_pk_mul_f32 v[52:53], v[52:53], v[134:135]
	v_add_co_u32_e32 v134, vcc, s78, v140
	v_pk_mul_f32 v[50:51], v[50:51], v[142:143]
	s_nop 0
	v_addc_co_u32_e32 v135, vcc, 0, v141, vcc
	v_add_co_u32_e32 v142, vcc, s79, v140
	s_waitcnt vmcnt(23)
	v_mov_b64_e32 v[134:135], v[156:157]
	s_nop 0
	v_addc_co_u32_e32 v143, vcc, 0, v141, vcc
	s_waitcnt vmcnt(22)
	v_mov_b64_e32 v[136:137], v[158:159]
	v_lshl_add_u64 v[144:145], v[140:141], 0, s[30:31]
	v_lshlrev_b32_e32 v148, 16, v134
	v_and_b32_e32 v149, 0xffff0000, v134
	v_lshlrev_b32_e32 v146, 16, v136
	v_and_b32_e32 v136, 0xffff0000, v136
	v_lshlrev_b32_e32 v134, 16, v137
	v_rcp_f32_e32 v147, v136
	v_rcp_f32_e32 v136, v134
	v_and_b32_e32 v134, 0xffff0000, v137
	v_rcp_f32_e32 v137, v134
	v_lshlrev_b32_e32 v134, 16, v135
	v_and_b32_e32 v135, 0xffff0000, v135
	v_rcp_f32_e32 v146, v146
	v_pk_mul_f32 v[134:135], v[136:137], v[134:135]
	v_pk_mul_f32 v[146:147], v[146:147], v[148:149]
	v_pk_mul_f32 v[48:49], v[48:49], v[134:135]
	s_waitcnt vmcnt(21)
	v_mov_b64_e32 v[134:135], v[160:161]
	s_waitcnt vmcnt(20)
	v_mov_b64_e32 v[136:137], v[162:163]
	v_pk_mul_f32 v[46:47], v[46:47], v[146:147]
	v_lshlrev_b32_e32 v148, 16, v134
	v_lshlrev_b32_e32 v146, 16, v136
	v_and_b32_e32 v136, 0xffff0000, v136
	v_and_b32_e32 v149, 0xffff0000, v134
	v_lshlrev_b32_e32 v134, 16, v137
	v_rcp_f32_e32 v147, v136
	v_rcp_f32_e32 v136, v134
	v_and_b32_e32 v134, 0xffff0000, v137
	v_rcp_f32_e32 v137, v134
	v_lshlrev_b32_e32 v134, 16, v135
	v_and_b32_e32 v135, 0xffff0000, v135
	v_rcp_f32_e32 v146, v146
	v_pk_mul_f32 v[134:135], v[136:137], v[134:135]
	v_pk_mul_f32 v[146:147], v[146:147], v[148:149]
	v_pk_mul_f32 v[44:45], v[44:45], v[134:135]
	s_waitcnt vmcnt(19)
	v_mov_b64_e32 v[134:135], v[164:165]
	s_waitcnt vmcnt(18)
; __device__ __forceinline__ float bf_lo(unsigned w) { return __uint_as_float(w << 16); }
; __device__ __forceinline__ float bf_hi(unsigned w) { return __uint_as_float(w & 0xffff0000u); }
;     __device__ __forceinline__ void mid(f32x4 (&acc)[2][2][4][2], const Unit& u, int wr, int wc) const {
;     ...
;             for (int m = 0; m < 4; ++m) { const size_t r = (size_t)(row0 + ai * HALF + m * 16);
; #pragma unroll
;                 for (int bj = 0; bj < 2; ++bj)
; #pragma unroll
;                     for (int n = 0; n < 2; ++n) { const u32x2 ga = *(const u32x2*)(G + r * ldg + col0 + bj * HALF + n * 16), gb = *(const u32x2*)(G + r * ldg + 4096 + col0 + bj * HALF + n * 16); f32x4 a = acc[ai][bj][m][n];
;                         a[0] *= bf_lo(ga.x) * __builtin_amdgcn_rcpf(bf_lo(gb.x)); a[1] *= bf_hi(ga.x) * __builtin_amdgcn_rcpf(bf_hi(gb.x)); a[2] *= bf_lo(ga.y) * __builtin_amdgcn_rcpf(bf_lo(gb.y)); a[3] *= bf_hi(ga.y) * __builtin_amdgcn_rcpf(bf_hi(gb.y));
;                         acc[ai][bj][m][n] = a; }
	v_mov_b64_e32 v[136:137], v[166:167]
	v_pk_mul_f32 v[42:43], v[42:43], v[146:147]
	v_lshlrev_b32_e32 v148, 16, v134
	v_lshlrev_b32_e32 v146, 16, v136
	v_and_b32_e32 v136, 0xffff0000, v136
	v_and_b32_e32 v149, 0xffff0000, v134
	v_lshlrev_b32_e32 v134, 16, v137
	v_rcp_f32_e32 v147, v136
	v_rcp_f32_e32 v136, v134
	v_and_b32_e32 v134, 0xffff0000, v137
	v_rcp_f32_e32 v137, v134
	v_lshlrev_b32_e32 v134, 16, v135
	v_and_b32_e32 v135, 0xffff0000, v135
	v_rcp_f32_e32 v146, v146
	v_pk_mul_f32 v[134:135], v[136:137], v[134:135]
	v_pk_mul_f32 v[146:147], v[146:147], v[148:149]
	v_pk_mul_f32 v[40:41], v[40:41], v[134:135]
	s_waitcnt vmcnt(17)
	v_mov_b64_e32 v[134:135], v[168:169]
	s_waitcnt vmcnt(16)
	v_mov_b64_e32 v[136:137], v[170:171]
	v_pk_mul_f32 v[38:39], v[38:39], v[146:147]
	v_lshlrev_b32_e32 v144, 16, v134
	v_lshlrev_b32_e32 v142, 16, v136
	v_and_b32_e32 v136, 0xffff0000, v136
	v_and_b32_e32 v145, 0xffff0000, v134
	v_lshlrev_b32_e32 v134, 16, v137
	v_rcp_f32_e32 v143, v136
	v_rcp_f32_e32 v136, v134
	v_and_b32_e32 v134, 0xffff0000, v137
	v_rcp_f32_e32 v137, v134
	v_rcp_f32_e32 v142, v142
	v_lshlrev_b32_e32 v134, 16, v135
	v_and_b32_e32 v135, 0xffff0000, v135
	v_pk_mul_f32 v[134:135], v[136:137], v[134:135]
	v_pk_mul_f32 v[142:143], v[142:143], v[144:145]
	v_pk_mul_f32 v[36:37], v[36:37], v[134:135]
	v_add_co_u32_e32 v134, vcc, s80, v140
	v_pk_mul_f32 v[34:35], v[34:35], v[142:143]
	s_nop 0
	v_addc_co_u32_e32 v135, vcc, 0, v141, vcc
	v_add_co_u32_e32 v142, vcc, s81, v140
	s_waitcnt vmcnt(15)
	v_mov_b64_e32 v[134:135], v[172:173]
	s_nop 0
	v_addc_co_u32_e32 v143, vcc, 0, v141, vcc
	s_waitcnt vmcnt(14)
	v_mov_b64_e32 v[136:137], v[174:175]
	v_lshl_add_u64 v[144:145], v[140:141], 0, s[38:39]
	v_lshlrev_b32_e32 v148, 16, v134
	v_and_b32_e32 v149, 0xffff0000, v134
	v_lshlrev_b32_e32 v146, 16, v136
	v_and_b32_e32 v136, 0xffff0000, v136
	v_lshlrev_b32_e32 v134, 16, v137
	v_rcp_f32_e32 v147, v136
	v_rcp_f32_e32 v136, v134
	v_and_b32_e32 v134, 0xffff0000, v137
	v_rcp_f32_e32 v137, v134
	v_lshlrev_b32_e32 v134, 16, v135
	v_and_b32_e32 v135, 0xffff0000, v135
	v_rcp_f32_e32 v146, v146
	v_pk_mul_f32 v[134:135], v[136:137], v[134:135]
	v_pk_mul_f32 v[146:147], v[146:147], v[148:149]
	v_pk_mul_f32 v[32:33], v[32:33], v[134:135]
	s_waitcnt vmcnt(13)
	v_mov_b64_e32 v[134:135], v[176:177]
	s_waitcnt vmcnt(12)
	v_mov_b64_e32 v[136:137], v[178:179]
	v_pk_mul_f32 v[30:31], v[30:31], v[146:147]
	v_lshlrev_b32_e32 v148, 16, v134
	v_lshlrev_b32_e32 v146, 16, v136
	v_and_b32_e32 v136, 0xffff0000, v136
	v_and_b32_e32 v149, 0xffff0000, v134
	v_lshlrev_b32_e32 v134, 16, v137
	v_rcp_f32_e32 v147, v136
	v_rcp_f32_e32 v136, v134
	v_and_b32_e32 v134, 0xffff0000, v137
	v_rcp_f32_e32 v137, v134
	v_lshlrev_b32_e32 v134, 16, v135
	v_and_b32_e32 v135, 0xffff0000, v135
	v_rcp_f32_e32 v146, v146
	v_pk_mul_f32 v[134:135], v[136:137], v[134:135]
	v_pk_mul_f32 v[146:147], v[146:147], v[148:149]
	v_pk_mul_f32 v[28:29], v[28:29], v[134:135]
	s_waitcnt vmcnt(11)
	v_mov_b64_e32 v[134:135], v[180:181]
	s_waitcnt vmcnt(10)
	v_mov_b64_e32 v[136:137], v[182:183]
	v_pk_mul_f32 v[26:27], v[26:27], v[146:147]
	v_lshlrev_b32_e32 v148, 16, v134
	v_lshlrev_b32_e32 v146, 16, v136
	v_and_b32_e32 v136, 0xffff0000, v136
	v_and_b32_e32 v149, 0xffff0000, v134
	v_lshlrev_b32_e32 v134, 16, v137
	v_rcp_f32_e32 v147, v136
	v_rcp_f32_e32 v136, v134
	v_and_b32_e32 v134, 0xffff0000, v137
	v_rcp_f32_e32 v137, v134
	v_lshlrev_b32_e32 v134, 16, v135
	v_and_b32_e32 v135, 0xffff0000, v135
	v_rcp_f32_e32 v146, v146
	v_pk_mul_f32 v[134:135], v[136:137], v[134:135]
	v_pk_mul_f32 v[146:147], v[146:147], v[148:149]
	v_pk_mul_f32 v[24:25], v[24:25], v[134:135]
	s_waitcnt vmcnt(9)
	v_mov_b64_e32 v[134:135], v[184:185]
	s_waitcnt vmcnt(8)
; __device__ __forceinline__ float bf_lo(unsigned w) { return __uint_as_float(w << 16); }
; __device__ __forceinline__ float bf_hi(unsigned w) { return __uint_as_float(w & 0xffff0000u); }
;     __device__ __forceinline__ void mid(f32x4 (&acc)[2][2][4][2], const Unit& u, int wr, int wc) const {
;     ...
;             for (int m = 0; m < 4; ++m) { const size_t r = (size_t)(row0 + ai * HALF + m * 16);
; #pragma unroll
;                 for (int bj = 0; bj < 2; ++bj)
; #pragma unroll
;                     for (int n = 0; n < 2; ++n) { const u32x2 ga = *(const u32x2*)(G + r * ldg + col0 + bj * HALF + n * 16), gb = *(const u32x2*)(G + r * ldg + 4096 + col0 + bj * HALF + n * 16); f32x4 a = acc[ai][bj][m][n];
;                         a[0] *= bf_lo(ga.x) * __builtin_amdgcn_rcpf(bf_lo(gb.x)); a[1] *= bf_hi(ga.x) * __builtin_amdgcn_rcpf(bf_hi(gb.x)); a[2] *= bf_lo(ga.y) * __builtin_amdgcn_rcpf(bf_lo(gb.y)); a[3] *= bf_hi(ga.y) * __builtin_amdgcn_rcpf(bf_hi(gb.y));
;                         acc[ai][bj][m][n] = a; }
;                 asm volatile("" ::: "memory"); }
	v_mov_b64_e32 v[136:137], v[186:187]
	v_pk_mul_f32 v[22:23], v[22:23], v[146:147]
	v_lshlrev_b32_e32 v144, 16, v134
	v_lshlrev_b32_e32 v142, 16, v136
	v_and_b32_e32 v136, 0xffff0000, v136
	v_and_b32_e32 v145, 0xffff0000, v134
	v_lshlrev_b32_e32 v134, 16, v137
	v_rcp_f32_e32 v143, v136
	v_rcp_f32_e32 v136, v134
	v_and_b32_e32 v134, 0xffff0000, v137
	v_rcp_f32_e32 v137, v134
	v_rcp_f32_e32 v142, v142
	v_lshlrev_b32_e32 v134, 16, v135
	v_and_b32_e32 v135, 0xffff0000, v135
	v_pk_mul_f32 v[134:135], v[136:137], v[134:135]
	v_pk_mul_f32 v[142:143], v[142:143], v[144:145]
	v_pk_mul_f32 v[20:21], v[20:21], v[134:135]
	v_add_co_u32_e32 v134, vcc, s82, v140
	v_pk_mul_f32 v[18:19], v[18:19], v[142:143]
	s_nop 0
	v_addc_co_u32_e32 v135, vcc, 0, v141, vcc
	v_add_co_u32_e32 v142, vcc, s83, v140
	s_waitcnt vmcnt(7)
	v_mov_b64_e32 v[134:135], v[188:189]
	s_nop 0
	v_addc_co_u32_e32 v143, vcc, 0, v141, vcc
	s_waitcnt vmcnt(6)
	v_mov_b64_e32 v[136:137], v[190:191]
	v_lshl_add_u64 v[144:145], v[140:141], 0, s[40:41]
	v_lshlrev_b32_e32 v146, 16, v134
	v_and_b32_e32 v147, 0xffff0000, v134
	v_lshlrev_b32_e32 v140, 16, v136
	v_and_b32_e32 v136, 0xffff0000, v136
	v_lshlrev_b32_e32 v134, 16, v137
	v_rcp_f32_e32 v141, v136
	v_rcp_f32_e32 v136, v134
	v_and_b32_e32 v134, 0xffff0000, v137
	v_rcp_f32_e32 v137, v134
	v_lshlrev_b32_e32 v134, 16, v135
	v_and_b32_e32 v135, 0xffff0000, v135
	v_rcp_f32_e32 v140, v140
	v_pk_mul_f32 v[134:135], v[136:137], v[134:135]
	v_pk_mul_f32 v[140:141], v[140:141], v[146:147]
	v_pk_mul_f32 v[16:17], v[16:17], v[134:135]
	s_waitcnt vmcnt(5)
	v_mov_b64_e32 v[134:135], v[192:193]
	s_waitcnt vmcnt(4)
	v_mov_b64_e32 v[136:137], v[194:195]
	v_pk_mul_f32 v[14:15], v[14:15], v[140:141]
	v_lshlrev_b32_e32 v146, 16, v134
	v_lshlrev_b32_e32 v140, 16, v136
	v_and_b32_e32 v136, 0xffff0000, v136
	v_and_b32_e32 v147, 0xffff0000, v134
	v_lshlrev_b32_e32 v134, 16, v137
	v_rcp_f32_e32 v141, v136
	v_rcp_f32_e32 v136, v134
	v_and_b32_e32 v134, 0xffff0000, v137
	v_rcp_f32_e32 v137, v134
	v_lshlrev_b32_e32 v134, 16, v135
	v_and_b32_e32 v135, 0xffff0000, v135
	v_rcp_f32_e32 v140, v140
	v_pk_mul_f32 v[134:135], v[136:137], v[134:135]
	v_pk_mul_f32 v[140:141], v[140:141], v[146:147]
	v_pk_mul_f32 v[12:13], v[12:13], v[134:135]
	s_waitcnt vmcnt(3)
	v_mov_b64_e32 v[134:135], v[196:197]
	s_waitcnt vmcnt(2)
	v_mov_b64_e32 v[136:137], v[198:199]
	v_pk_mul_f32 v[10:11], v[10:11], v[140:141]
	v_lshlrev_b32_e32 v146, 16, v134
	v_lshlrev_b32_e32 v140, 16, v136
	v_and_b32_e32 v136, 0xffff0000, v136
	v_rcp_f32_e32 v140, v140
	v_rcp_f32_e32 v141, v136
	v_and_b32_e32 v147, 0xffff0000, v134
	v_lshlrev_b32_e32 v134, 16, v137
	v_rcp_f32_e32 v136, v134
	v_pk_mul_f32 v[140:141], v[140:141], v[146:147]
	v_and_b32_e32 v134, 0xffff0000, v137
	v_pk_mul_f32 v[6:7], v[6:7], v[140:141]
	s_waitcnt vmcnt(1)
	v_mov_b64_e32 v[140:141], v[200:201]
	s_nop 0
	s_waitcnt vmcnt(0)
	v_mov_b64_e32 v[142:143], v[202:203]
	v_rcp_f32_e32 v137, v134
	v_lshlrev_b32_e32 v134, 16, v135
	v_and_b32_e32 v135, 0xffff0000, v135
	v_pk_mul_f32 v[134:135], v[136:137], v[134:135]
	v_lshlrev_b32_e32 v136, 16, v140
	v_pk_mul_f32 v[8:9], v[8:9], v[134:135]
	v_lshlrev_b32_e32 v134, 16, v142
	v_and_b32_e32 v135, 0xffff0000, v142
	v_rcp_f32_e32 v134, v134
	v_rcp_f32_e32 v135, v135
	v_and_b32_e32 v137, 0xffff0000, v140
	v_pk_mul_f32 v[134:135], v[134:135], v[136:137]
	s_nop 0
	v_pk_mul_f32 v[2:3], v[2:3], v[134:135]
	v_lshlrev_b32_e32 v134, 16, v143
	v_and_b32_e32 v135, 0xffff0000, v143
	v_rcp_f32_e32 v134, v134
	v_rcp_f32_e32 v135, v135
	v_lshlrev_b32_e32 v136, 16, v141
	v_and_b32_e32 v137, 0xffff0000, v141
	v_pk_mul_f32 v[134:135], v[134:135], v[136:137]
	s_nop 0
	v_pk_mul_f32 v[4:5], v[4:5], v[134:135]
	s_branch .LBB0_2989
